# speedup vs baseline: 1.0373x; 1.0029x over previous
.LBB0_8:
	s_and_b64 vcc, exec, s[4:5]
	s_cbranch_vccz .LBB0_44
	s_load_dwordx16 s[4:19], s[0:1], 0x30
	s_load_dwordx2 s[28:29], s[0:1], 0x90
	s_load_dwordx8 s[20:27], s[0:1], 0x70
	s_lshl_b32 s33, s2, 9
	s_sub_u32 s2, s2, 0x100
	v_or_b32_e32 v1, s33, v0
	v_add_u32_e32 v2, 0xfffe0000, v1
	v_lshlrev_b32_e32 v3, 6, v2
	v_lshrrev_b32_e32 v4, 5, v2
	v_and_b32_e32 v3, 0x3e00, v3
	v_and_b32_e32 v4, 0x1f8, v4
	v_and_b32_e32 v5, 0xffffc007, v2
	v_or3_b32 v20, v5, v3, v4
	v_lshlrev_b32_e32 v20, 2, v20
	v_add_u32_e32 v6, 0x18000, v2
	v_lshlrev_b32_e32 v3, 6, v6
	v_lshrrev_b32_e32 v4, 5, v6
	v_and_b32_e32 v3, 0x3e00, v3
	v_and_b32_e32 v4, 0x1f8, v4
	v_and_b32_e32 v5, 0xffffc007, v6
	v_or3_b32 v21, v5, v3, v4
	v_lshlrev_b32_e32 v21, 2, v21
	v_and_b32_e32 v7, 0xffff, v2
	v_add_u32_e32 v6, 0x30000, v7
	v_lshlrev_b32_e32 v3, 6, v6
	v_lshrrev_b32_e32 v4, 5, v6
	v_and_b32_e32 v3, 0x3e00, v3
	v_and_b32_e32 v4, 0x1f8, v4
	v_and_b32_e32 v5, 0xffffc007, v6
	v_or3_b32 v22, v5, v3, v4
	v_lshlrev_b32_e32 v22, 2, v22
	v_lshlrev_b32_e32 v3, 4, v7
	v_lshrrev_b32_e32 v4, 4, v7
	v_and_b32_e32 v3, 0x780, v3
	v_and_b32_e32 v4, 0x78, v4
	v_and_b32_e32 v5, 0xf807, v7
	v_or3_b32 v23, v5, v3, v4
	v_lshlrev_b32_e32 v23, 2, v23
	v_and_b32_e32 v6, 0x7fff, v2
	v_lshlrev_b32_e32 v3, 5, v6
	v_lshrrev_b32_e32 v4, 5, v6
	v_and_b32_e32 v3, 0x1f00, v3
	v_and_b32_e32 v4, 0xf8, v4
	v_and_b32_e32 v5, 0xe007, v6
	v_or3_b32 v24, v5, v3, v4
	v_lshlrev_b32_e32 v24, 2, v24
	v_and_b32_e32 v6, 0x3fff, v2
	v_lshrrev_b32_e32 v3, 8, v6
	v_lshrrev_b32_e32 v4, 3, v6
	v_and_b32_e32 v3, 0xf0, v3
	v_and_b32_e32 v4, 15, v4
	v_or_b32_e32 v3, v3, v4
	v_cmp_gt_u32_e64 s[30:31], 40, v3
	v_lshlrev_b32_e32 v3, 8, v3
	v_lshrrev_b32_e32 v4, 4, v6
	v_and_b32_e32 v4, 0xf8, v4
	v_and_b32_e32 v5, 7, v6
	v_or3_b32 v25, v3, v4, v5
	v_lshlrev_b32_e32 v25, 2, v25
	v_cndmask_b32_e64 v25, 0, v25, s[30:31]
	v_and_b32_e32 v26, 0xfff, v2
	v_lshlrev_b32_e32 v26, 2, v26
	v_lshlrev_b32_e32 v40, 1, v2
	v_add_u32_e32 v41, 0x30000, v40
	v_add_u32_e32 v42, 0x60000, v40
	v_lshlrev_b32_e32 v43, 2, v2
	v_mov_b32_e32 v44, 0
	s_waitcnt lgkmcnt(0)
	global_load_dword v30, v20, s[10:11] nt
	global_load_dword v31, v20, s[12:13] nt
	global_load_dword v32, v21, s[10:11] nt
	global_load_dword v33, v21, s[12:13] nt
	global_load_dword v34, v22, s[10:11] nt
	global_load_dword v35, v22, s[12:13] nt
	global_load_dword v36, v23, s[4:5] nt
	global_load_dword v37, v24, s[8:9] nt
	global_load_dword v38, v25, s[6:7] nt
	global_load_dword v39, v26, s[14:15] nt
	s_mov_b32 s6, 0x3fb8aa3b
	s_mov_b32 s7, 0xc2ce8ed0
	s_mov_b32 s8, 0x42b17218
	v_mov_b32_e32 v45, 0x7f800000
	s_waitcnt vmcnt(0)
	v_cvt_f16_f32_e32 v30, v30
	v_cvt_f16_f32_e32 v31, v31
	v_cvt_f16_f32_e32 v32, v32
	v_cvt_f16_f32_e32 v33, v33
	global_store_short v40, v30, s[22:23]
	global_store_short v40, v31, s[24:25]
	global_store_short v41, v32, s[22:23]
	global_store_short v41, v33, s[24:25]
	s_cmp_lt_u32 s2, 0x80
	s_cbranch_scc0 .LBB0_44
	v_cvt_f16_f32_e32 v34, v34
	v_cvt_f16_f32_e32 v35, v35
	v_cvt_f16_f32_e32 v36, v36
	global_store_short v42, v34, s[22:23]
	global_store_short v42, v35, s[24:25]
	global_store_short v40, v36, s[16:17]
	s_cmp_lt_u32 s2, 64
	s_cbranch_scc0 .LBB0_44
	v_cvt_f16_f32_e32 v37, v37
	global_store_short v40, v37, s[20:21]
	s_cmp_lt_u32 s2, 32
	s_cbranch_scc0 .LBB0_44
	global_store_dword v43, v44, s[28:29]
	s_cmp_lt_u32 s2, 24
	s_cbranch_scc0 .LBB0_44
	v_cvt_f16_f32_e32 v38, v38
	s_nop 0
	v_cndmask_b32_e64 v38, 0, v38, s[30:31]
	global_store_short v40, v38, s[18:19]
	s_cmp_lt_u32 s2, 8
	s_cbranch_scc0 .LBB0_44
	v_mul_f32_e32 v9, 0x3fb8aa3b, v39
	v_rndne_f32_e32 v10, v9
	v_fma_f32 v11, v39, s6, -v9
	v_sub_f32_e32 v9, v9, v10
	v_fmac_f32_e32 v11, 0x32a5705f, v39
	v_add_f32_e32 v9, v9, v11
	v_cvt_i32_f32_e32 v10, v10
	v_exp_f32_e32 v9, v9
	v_cmp_ngt_f32_e32 vcc, s7, v39
	v_ldexp_f32 v9, v9, v10
	s_nop 0
	v_cndmask_b32_e32 v9, 0, v9, vcc
	v_cmp_nlt_f32_e32 vcc, s8, v39
	s_nop 1
	v_cndmask_b32_e32 v8, v45, v9, vcc
	v_mul_f32_e32 v8, 0xbfb8aa3b, v8
	global_store_dword v43, v8, s[26:27]
